# v79 + k3 K-loop L2 look-ahead touch loads (1 dword per 128B line, ~1.5 tiles ahead of the LDS-DMA), counted vmcnt +1/+2
# baseline (speedup 1.0000x reference)
.LBB0_798:
	s_add_u32 s8, s40, 0x100080
	s_addc_u32 s9, s41, 0
	s_add_u32 s70, s36, 0x100
	v_mov_b32_e32 v2, 0
	v_lshl_add_u64 v[212:213], s[8:9], 0, v[208:209]
	v_lshl_add_u64 v[214:215], s[8:9], 0, v[210:211]
	s_addc_u32 s71, s37, 0
	v_readfirstlane_b32 s16, v0
	v_and_b32_e32 v230, 0xff, v0
	s_cmpk_lt_u32 s16, 0x100
	s_cselect_b32 s18, s40, s36
	s_cselect_b32 s19, s41, s37
	s_cselect_b32 s17, 13, 11
	v_lshlrev_b32_e32 v230, s17, v230
	v_mov_b32_e32 v231, 0
	s_add_u32 s18, s18, 0x100
	s_addc_u32 s19, s19, 0
	v_lshl_add_u64 v[230:231], s[18:19], 0, v[230:231]
	s_movk_i32 s16, 0x80
	s_mov_b32 s17, 0
	global_load_dword v227, v[230:231], off
	v_lshl_add_u64 v[230:231], v[230:231], 0, s[16:17]
	s_movk_i32 s16, 0x100
	s_mov_b32 s8, -2
	s_mov_b64 s[58:59], 0
	s_xor_b64 s[64:65], s[64:65], -1
	v_mov_b32_e32 v3, v2
	v_mov_b32_e32 v4, v2
	v_mov_b32_e32 v5, v2
	v_mov_b32_e32 v6, v2
	v_mov_b32_e32 v7, v2
	v_mov_b32_e32 v8, v2
	v_mov_b32_e32 v9, v2
	v_mov_b32_e32 v18, v2
	v_mov_b32_e32 v19, v2
	v_mov_b32_e32 v20, v2
	v_mov_b32_e32 v21, v2
	v_mov_b32_e32 v22, v2
	v_mov_b32_e32 v23, v2
	v_mov_b32_e32 v24, v2
	v_mov_b32_e32 v25, v2
	v_mov_b32_e32 v34, v2
	v_mov_b32_e32 v35, v2
	v_mov_b32_e32 v36, v2
	v_mov_b32_e32 v37, v2
	v_mov_b32_e32 v38, v2
	v_mov_b32_e32 v39, v2
	v_mov_b32_e32 v40, v2
	v_mov_b32_e32 v41, v2
	v_mov_b32_e32 v50, v2
	v_mov_b32_e32 v51, v2
	v_mov_b32_e32 v52, v2
	v_mov_b32_e32 v53, v2
	v_mov_b32_e32 v54, v2
	v_mov_b32_e32 v55, v2
	v_mov_b32_e32 v56, v2
	v_mov_b32_e32 v57, v2
	v_mov_b32_e32 v10, v2
	v_mov_b32_e32 v11, v2
	v_mov_b32_e32 v12, v2
	v_mov_b32_e32 v13, v2
	v_mov_b32_e32 v14, v2
	v_mov_b32_e32 v15, v2
	v_mov_b32_e32 v16, v2
	v_mov_b32_e32 v17, v2
	v_mov_b32_e32 v26, v2
	v_mov_b32_e32 v27, v2
	v_mov_b32_e32 v28, v2
	v_mov_b32_e32 v29, v2
	v_mov_b32_e32 v30, v2
	v_mov_b32_e32 v31, v2
	v_mov_b32_e32 v32, v2
	v_mov_b32_e32 v33, v2
	v_mov_b32_e32 v42, v2
	v_mov_b32_e32 v43, v2
	v_mov_b32_e32 v44, v2
	v_mov_b32_e32 v45, v2
	v_mov_b32_e32 v46, v2
	v_mov_b32_e32 v47, v2
	v_mov_b32_e32 v48, v2
	v_mov_b32_e32 v49, v2
	v_mov_b32_e32 v58, v2
	v_mov_b32_e32 v59, v2
	v_mov_b32_e32 v60, v2
	v_mov_b32_e32 v61, v2
	v_mov_b32_e32 v62, v2
	v_mov_b32_e32 v63, v2
	v_mov_b32_e32 v64, v2
	v_mov_b32_e32 v65, v2
	v_mov_b32_e32 v68, v2
	v_mov_b32_e32 v69, v2
	v_mov_b32_e32 v70, v2
	v_mov_b32_e32 v71, v2
	v_mov_b32_e32 v72, v2
	v_mov_b32_e32 v73, v2
	v_mov_b32_e32 v74, v2
	v_mov_b32_e32 v75, v2
	v_mov_b32_e32 v84, v2
	v_mov_b32_e32 v85, v2
	v_mov_b32_e32 v86, v2
	v_mov_b32_e32 v87, v2
	v_mov_b32_e32 v88, v2
	v_mov_b32_e32 v89, v2
	v_mov_b32_e32 v90, v2
	v_mov_b32_e32 v91, v2
	v_mov_b32_e32 v100, v2
	v_mov_b32_e32 v101, v2
	v_mov_b32_e32 v102, v2
	v_mov_b32_e32 v103, v2
	v_mov_b32_e32 v104, v2
	v_mov_b32_e32 v105, v2
	v_mov_b32_e32 v106, v2
	v_mov_b32_e32 v107, v2
	v_mov_b32_e32 v116, v2
	v_mov_b32_e32 v117, v2
	v_mov_b32_e32 v118, v2
	v_mov_b32_e32 v119, v2
	v_mov_b32_e32 v120, v2
	v_mov_b32_e32 v121, v2
	v_mov_b32_e32 v122, v2
	v_mov_b32_e32 v123, v2
	v_mov_b32_e32 v76, v2
	v_mov_b32_e32 v77, v2
	v_mov_b32_e32 v78, v2
	v_mov_b32_e32 v79, v2
	v_mov_b32_e32 v80, v2
	v_mov_b32_e32 v81, v2
	v_mov_b32_e32 v82, v2
	v_mov_b32_e32 v83, v2
	v_mov_b32_e32 v92, v2
	v_mov_b32_e32 v93, v2
	v_mov_b32_e32 v94, v2
	v_mov_b32_e32 v95, v2
	v_mov_b32_e32 v96, v2
	v_mov_b32_e32 v97, v2
	v_mov_b32_e32 v98, v2
	v_mov_b32_e32 v99, v2
	v_mov_b32_e32 v108, v2
	v_mov_b32_e32 v109, v2
	v_mov_b32_e32 v110, v2
	v_mov_b32_e32 v111, v2
	v_mov_b32_e32 v112, v2
	v_mov_b32_e32 v113, v2
	v_mov_b32_e32 v114, v2
	v_mov_b32_e32 v115, v2
	v_mov_b32_e32 v124, v2
	v_mov_b32_e32 v125, v2
	v_mov_b32_e32 v126, v2
	v_mov_b32_e32 v127, v2
	v_mov_b32_e32 v128, v2
	v_mov_b32_e32 v129, v2
	v_mov_b32_e32 v130, v2
	v_mov_b32_e32 v131, v2
	s_branch .LBB0_800
.LBB0_799:
	s_waitcnt lgkmcnt(0)
	s_barrier
	s_setprio 1
	s_waitcnt lgkmcnt(0)
	v_mfma_f32_16x16x32_bf16 v[62:65], v[148:151], v[188:191], v[62:65]
	v_mfma_f32_16x16x32_bf16 v[58:61], v[156:159], v[188:191], v[58:61]
	v_mfma_f32_16x16x32_bf16 v[46:49], v[148:151], v[180:183], v[46:49]
	v_mfma_f32_16x16x32_bf16 v[42:45], v[156:159], v[180:183], v[42:45]
	v_mfma_f32_16x16x32_bf16 v[30:33], v[148:151], v[172:175], v[30:33]
	v_mfma_f32_16x16x32_bf16 v[26:29], v[156:159], v[172:175], v[26:29]
	v_mfma_f32_16x16x32_bf16 v[14:17], v[148:151], v[164:167], v[14:17]
	v_mfma_f32_16x16x32_bf16 v[10:13], v[156:159], v[164:167], v[10:13]
	v_mfma_f32_16x16x32_bf16 v[62:65], v[152:155], v[192:195], v[62:65]
	v_mfma_f32_16x16x32_bf16 v[58:61], v[160:163], v[192:195], v[58:61]
	v_mfma_f32_16x16x32_bf16 v[46:49], v[152:155], v[184:187], v[46:49]
	v_mfma_f32_16x16x32_bf16 v[42:45], v[160:163], v[184:187], v[42:45]
	v_mfma_f32_16x16x32_bf16 v[30:33], v[152:155], v[176:179], v[30:33]
	v_mfma_f32_16x16x32_bf16 v[26:29], v[160:163], v[176:179], v[26:29]
	v_mfma_f32_16x16x32_bf16 v[14:17], v[152:155], v[168:171], v[14:17]
	v_mfma_f32_16x16x32_bf16 v[10:13], v[160:163], v[168:171], v[10:13]
	s_setprio 0
	s_setprio 1
	v_mfma_f32_16x16x32_bf16 v[54:57], v[132:135], v[188:191], v[54:57]
	v_mfma_f32_16x16x32_bf16 v[50:53], v[140:143], v[188:191], v[50:53]
	v_mfma_f32_16x16x32_bf16 v[38:41], v[132:135], v[180:183], v[38:41]
	v_mfma_f32_16x16x32_bf16 v[34:37], v[140:143], v[180:183], v[34:37]
	v_mfma_f32_16x16x32_bf16 v[22:25], v[132:135], v[172:175], v[22:25]
	v_mfma_f32_16x16x32_bf16 v[18:21], v[140:143], v[172:175], v[18:21]
	v_mfma_f32_16x16x32_bf16 v[6:9], v[132:135], v[164:167], v[6:9]
	v_mfma_f32_16x16x32_bf16 v[2:5], v[140:143], v[164:167], v[2:5]
	v_mfma_f32_16x16x32_bf16 v[54:57], v[136:139], v[192:195], v[54:57]
	v_mfma_f32_16x16x32_bf16 v[50:53], v[144:147], v[192:195], v[50:53]
	v_mfma_f32_16x16x32_bf16 v[38:41], v[136:139], v[184:187], v[38:41]
	v_mfma_f32_16x16x32_bf16 v[34:37], v[144:147], v[184:187], v[34:37]
	v_mfma_f32_16x16x32_bf16 v[22:25], v[136:139], v[176:179], v[22:25]
	v_mfma_f32_16x16x32_bf16 v[18:21], v[144:147], v[176:179], v[18:21]
	v_mfma_f32_16x16x32_bf16 v[6:9], v[136:139], v[168:171], v[6:9]
	v_mfma_f32_16x16x32_bf16 v[2:5], v[144:147], v[168:171], v[2:5]
	s_setprio 0
	s_barrier
	s_add_i32 s9, 0, 0x18000
	s_add_i32 s12, 0, 0x1c000
	v_add_u32_e32 v144, s9, v225
	v_add_u32_e32 v160, s12, v225
	ds_read_b128 v[132:135], v144
	ds_read_b128 v[136:139], v144 offset:1024
	ds_read_b128 v[140:143], v144 offset:2048
	ds_read_b128 v[144:147], v144 offset:3072
	ds_read_b128 v[148:151], v160
	ds_read_b128 v[152:155], v160 offset:1024
	ds_read_b128 v[156:159], v160 offset:2048
	ds_read_b128 v[160:163], v160 offset:3072
	s_add_u32 s10, s66, 0x100000
	s_addc_u32 s11, s67, 0
	s_mov_b32 m0, s88
	v_lshl_add_u64 v[228:229], s[10:11], 0, v[196:197]
	ds_read_b128 v[164:167], v226 offset:32768
	ds_read_b128 v[168:171], v226 offset:33792
	ds_read_b128 v[172:175], v226 offset:34816
	ds_read_b128 v[176:179], v226 offset:35840
	ds_read_b128 v[180:183], v226 offset:36864
	ds_read_b128 v[184:187], v226 offset:37888
	ds_read_b128 v[188:191], v226 offset:38912
	ds_read_b128 v[192:195], v226 offset:39936
	global_load_lds_dwordx4 v[228:229], off
	v_lshl_add_u64 v[228:229], s[10:11], 0, v[200:201]
	s_mov_b32 m0, s89
	s_nop 0
	global_load_lds_dwordx4 v[228:229], off
	s_waitcnt vmcnt(9)
	s_waitcnt lgkmcnt(0)
	s_barrier
	s_setprio 1
	s_waitcnt lgkmcnt(0)
	v_mfma_f32_16x16x32_bf16 v[128:131], v[132:135], v[164:167], v[128:131]
	v_mfma_f32_16x16x32_bf16 v[124:127], v[140:143], v[164:167], v[124:127]
	v_mfma_f32_16x16x32_bf16 v[112:115], v[132:135], v[172:175], v[112:115]
	v_mfma_f32_16x16x32_bf16 v[108:111], v[140:143], v[172:175], v[108:111]
	v_mfma_f32_16x16x32_bf16 v[96:99], v[132:135], v[180:183], v[96:99]
	v_mfma_f32_16x16x32_bf16 v[92:95], v[140:143], v[180:183], v[92:95]
	v_mfma_f32_16x16x32_bf16 v[80:83], v[132:135], v[188:191], v[80:83]
	v_mfma_f32_16x16x32_bf16 v[76:79], v[140:143], v[188:191], v[76:79]
	v_mfma_f32_16x16x32_bf16 v[128:131], v[136:139], v[168:171], v[128:131]
	v_mfma_f32_16x16x32_bf16 v[124:127], v[144:147], v[168:171], v[124:127]
	v_mfma_f32_16x16x32_bf16 v[112:115], v[136:139], v[176:179], v[112:115]
	v_mfma_f32_16x16x32_bf16 v[108:111], v[144:147], v[176:179], v[108:111]
	v_mfma_f32_16x16x32_bf16 v[96:99], v[136:139], v[184:187], v[96:99]
	v_mfma_f32_16x16x32_bf16 v[92:95], v[144:147], v[184:187], v[92:95]
	v_mfma_f32_16x16x32_bf16 v[80:83], v[136:139], v[192:195], v[80:83]
	v_mfma_f32_16x16x32_bf16 v[76:79], v[144:147], v[192:195], v[76:79]
	s_setprio 0
	s_setprio 1
	v_mfma_f32_16x16x32_bf16 v[120:123], v[148:151], v[164:167], v[120:123]
	v_mfma_f32_16x16x32_bf16 v[116:119], v[156:159], v[164:167], v[116:119]
	v_mfma_f32_16x16x32_bf16 v[104:107], v[148:151], v[172:175], v[104:107]
	v_mfma_f32_16x16x32_bf16 v[100:103], v[156:159], v[172:175], v[100:103]
	v_mfma_f32_16x16x32_bf16 v[88:91], v[148:151], v[180:183], v[88:91]
	v_mfma_f32_16x16x32_bf16 v[84:87], v[156:159], v[180:183], v[84:87]
	v_mfma_f32_16x16x32_bf16 v[72:75], v[148:151], v[188:191], v[72:75]
	v_mfma_f32_16x16x32_bf16 v[68:71], v[156:159], v[188:191], v[68:71]
	v_mfma_f32_16x16x32_bf16 v[120:123], v[152:155], v[168:171], v[120:123]
	v_mfma_f32_16x16x32_bf16 v[116:119], v[160:163], v[168:171], v[116:119]
	v_mfma_f32_16x16x32_bf16 v[104:107], v[152:155], v[176:179], v[104:107]
	v_mfma_f32_16x16x32_bf16 v[100:103], v[160:163], v[176:179], v[100:103]
	v_mfma_f32_16x16x32_bf16 v[88:91], v[152:155], v[184:187], v[88:91]
	v_mfma_f32_16x16x32_bf16 v[84:87], v[160:163], v[184:187], v[84:87]
	v_mfma_f32_16x16x32_bf16 v[72:75], v[152:155], v[192:195], v[72:75]
	v_mfma_f32_16x16x32_bf16 v[68:71], v[160:163], v[192:195], v[68:71]
	s_setprio 0
	s_barrier
	s_add_i32 s9, s9, s72
	v_lshl_add_u64 v[222:223], v[222:223], 0, s[60:61]
	s_mov_b32 m0, s9
	ds_read_b128 v[164:167], v226 offset:49152
	ds_read_b128 v[168:171], v226 offset:50176
	ds_read_b128 v[172:175], v226 offset:51200
	ds_read_b128 v[176:179], v226 offset:52224
	ds_read_b128 v[180:183], v226 offset:53248
	ds_read_b128 v[184:187], v226 offset:54272
	ds_read_b128 v[188:191], v226 offset:55296
	ds_read_b128 v[192:195], v226 offset:56320
	global_load_lds_dwordx4 v[222:223], off
	s_add_i32 m0, s9, 0x2000
	s_add_u32 s10, s36, 0x40080
	v_lshl_add_u64 v[220:221], v[220:221], 0, s[60:61]
	s_addc_u32 s11, s37, 0
	s_add_i32 s9, s12, s72
	global_load_lds_dwordx4 v[220:221], off
	v_lshl_add_u64 v[220:221], s[10:11], 0, v[198:199]
	s_mov_b32 m0, s9
	v_lshl_add_u64 v[216:217], v[216:217], 0, s[60:61]
	global_load_lds_dwordx4 v[220:221], off
	v_lshl_add_u64 v[220:221], s[10:11], 0, v[202:203]
	s_add_i32 m0, s9, 0x2000
	s_nop 0
	global_load_lds_dwordx4 v[220:221], off
	s_mov_b32 m0, s91
	s_nop 0
	global_load_lds_dwordx4 v[216:217], off
	v_lshl_add_u64 v[216:217], v[218:219], 0, s[60:61]
	s_mov_b32 m0, s92
	s_nop 0
	global_load_lds_dwordx4 v[216:217], off
	global_load_dword v227, v[230:231], off offset:128
	v_lshl_add_u64 v[230:231], v[230:231], 0, s[16:17]
	s_waitcnt vmcnt(10)
	s_waitcnt lgkmcnt(0)
	s_barrier
	s_setprio 1
	s_waitcnt lgkmcnt(0)
	v_mfma_f32_16x16x32_bf16 v[62:65], v[132:135], v[164:167], v[62:65]
	v_mfma_f32_16x16x32_bf16 v[58:61], v[140:143], v[164:167], v[58:61]
	v_mfma_f32_16x16x32_bf16 v[46:49], v[132:135], v[172:175], v[46:49]
	v_mfma_f32_16x16x32_bf16 v[42:45], v[140:143], v[172:175], v[42:45]
	v_mfma_f32_16x16x32_bf16 v[30:33], v[132:135], v[180:183], v[30:33]
	v_mfma_f32_16x16x32_bf16 v[26:29], v[140:143], v[180:183], v[26:29]
	v_mfma_f32_16x16x32_bf16 v[14:17], v[132:135], v[188:191], v[14:17]
	v_mfma_f32_16x16x32_bf16 v[10:13], v[140:143], v[188:191], v[10:13]
	v_mfma_f32_16x16x32_bf16 v[62:65], v[136:139], v[168:171], v[62:65]
	v_mfma_f32_16x16x32_bf16 v[58:61], v[144:147], v[168:171], v[58:61]
	v_mfma_f32_16x16x32_bf16 v[46:49], v[136:139], v[176:179], v[46:49]
	v_mfma_f32_16x16x32_bf16 v[42:45], v[144:147], v[176:179], v[42:45]
	v_mfma_f32_16x16x32_bf16 v[30:33], v[136:139], v[184:187], v[30:33]
	v_mfma_f32_16x16x32_bf16 v[26:29], v[144:147], v[184:187], v[26:29]
	v_mfma_f32_16x16x32_bf16 v[14:17], v[136:139], v[192:195], v[14:17]
	v_mfma_f32_16x16x32_bf16 v[10:13], v[144:147], v[192:195], v[10:13]
	s_setprio 0
	s_setprio 1
	v_mfma_f32_16x16x32_bf16 v[54:57], v[148:151], v[164:167], v[54:57]
	v_mfma_f32_16x16x32_bf16 v[50:53], v[156:159], v[164:167], v[50:53]
	v_mfma_f32_16x16x32_bf16 v[38:41], v[148:151], v[172:175], v[38:41]
	v_mfma_f32_16x16x32_bf16 v[34:37], v[156:159], v[172:175], v[34:37]
	v_mfma_f32_16x16x32_bf16 v[22:25], v[148:151], v[180:183], v[22:25]
	v_mfma_f32_16x16x32_bf16 v[18:21], v[156:159], v[180:183], v[18:21]
	v_mfma_f32_16x16x32_bf16 v[6:9], v[148:151], v[188:191], v[6:9]
	v_mfma_f32_16x16x32_bf16 v[2:5], v[156:159], v[188:191], v[2:5]
	v_mfma_f32_16x16x32_bf16 v[54:57], v[152:155], v[168:171], v[54:57]
	v_mfma_f32_16x16x32_bf16 v[50:53], v[160:163], v[168:171], v[50:53]
	v_mfma_f32_16x16x32_bf16 v[38:41], v[152:155], v[176:179], v[38:41]
	v_mfma_f32_16x16x32_bf16 v[34:37], v[160:163], v[176:179], v[34:37]
	v_mfma_f32_16x16x32_bf16 v[22:25], v[152:155], v[184:187], v[22:25]
	v_mfma_f32_16x16x32_bf16 v[18:21], v[160:163], v[184:187], v[18:21]
	v_mfma_f32_16x16x32_bf16 v[6:9], v[152:155], v[192:195], v[6:9]
	v_mfma_f32_16x16x32_bf16 v[2:5], v[160:163], v[192:195], v[2:5]
	s_setprio 0
	s_barrier
	s_add_i32 s8, s8, 2
	s_add_u32 s58, s58, 0x100
	s_addc_u32 s59, s59, 0
	s_cmp_gt_u32 s8, 13
	s_cbranch_scc1 .LBB0_808
.LBB0_800:
	v_add_u32_e32 v132, 0, v225
	v_add_u32_e32 v133, 0x10000, v132
	v_add_u32_e32 v144, 0x14000, v132
	ds_read_b128 v[148:151], v133
	ds_read_b128 v[152:155], v133 offset:1024
	ds_read_b128 v[156:159], v133 offset:2048
	ds_read_b128 v[160:163], v133 offset:3072
	ds_read_b128 v[132:135], v144
	ds_read_b128 v[136:139], v144 offset:1024
	ds_read_b128 v[140:143], v144 offset:2048
	ds_read_b128 v[144:147], v144 offset:3072
	s_cmp_lg_u32 s58, 0
	s_cselect_b64 s[10:11], -1, 0
	s_mov_b64 s[26:27], -1
	s_or_b64 s[68:69], s[64:65], s[10:11]
	v_lshl_add_u64 v[216:217], v[212:213], 0, s[58:59]
	s_add_i32 m0, s74, 0xc000
	ds_read_b128 v[188:191], v226
	ds_read_b128 v[192:195], v226 offset:1024
	ds_read_b128 v[180:183], v226 offset:2048
	ds_read_b128 v[184:187], v226 offset:3072
	ds_read_b128 v[172:175], v226 offset:4096
	ds_read_b128 v[176:179], v226 offset:5120
	ds_read_b128 v[164:167], v226 offset:6144
	ds_read_b128 v[168:171], v226 offset:7168
	global_load_lds_dwordx4 v[216:217], off
	v_lshl_add_u64 v[216:217], v[214:215], 0, s[58:59]
	s_add_i32 m0, s74, 0xe000
	s_and_b64 vcc, exec, s[68:69]
	global_load_lds_dwordx4 v[216:217], off
	s_cbranch_vccz .LBB0_802
	s_waitcnt vmcnt(9)
	s_mov_b64 s[26:27], 0

.LBB0_804:
	s_add_u32 s9, s40, s58
	s_addc_u32 s10, s41, s59
	s_add_u32 s9, s9, 0x100
	s_addc_u32 s10, s10, 0
	s_add_u32 s11, s70, s58
	s_addc_u32 s12, s71, s59
	s_waitcnt lgkmcnt(0)
	s_cmpk_eq_i32 s58, 0x700
	s_cselect_b32 s67, s53, s10
	s_cselect_b32 s66, s52, s9
	s_cselect_b32 s37, s55, s12
	s_cselect_b32 s36, s54, s11
	s_barrier
	s_setprio 1
	s_waitcnt lgkmcnt(0)
	v_mfma_f32_16x16x32_bf16 v[128:131], v[148:151], v[188:191], v[128:131]
	v_mfma_f32_16x16x32_bf16 v[124:127], v[156:159], v[188:191], v[124:127]
	v_mfma_f32_16x16x32_bf16 v[112:115], v[148:151], v[180:183], v[112:115]
	v_mfma_f32_16x16x32_bf16 v[108:111], v[156:159], v[180:183], v[108:111]
	v_mfma_f32_16x16x32_bf16 v[96:99], v[148:151], v[172:175], v[96:99]
	v_mfma_f32_16x16x32_bf16 v[92:95], v[156:159], v[172:175], v[92:95]
	v_mfma_f32_16x16x32_bf16 v[80:83], v[148:151], v[164:167], v[80:83]
	v_mfma_f32_16x16x32_bf16 v[76:79], v[156:159], v[164:167], v[76:79]
	v_mfma_f32_16x16x32_bf16 v[128:131], v[152:155], v[192:195], v[128:131]
	v_mfma_f32_16x16x32_bf16 v[124:127], v[160:163], v[192:195], v[124:127]
	v_mfma_f32_16x16x32_bf16 v[112:115], v[152:155], v[184:187], v[112:115]
	v_mfma_f32_16x16x32_bf16 v[108:111], v[160:163], v[184:187], v[108:111]
	v_mfma_f32_16x16x32_bf16 v[96:99], v[152:155], v[176:179], v[96:99]
	v_mfma_f32_16x16x32_bf16 v[92:95], v[160:163], v[176:179], v[92:95]
	v_mfma_f32_16x16x32_bf16 v[80:83], v[152:155], v[168:171], v[80:83]
	v_mfma_f32_16x16x32_bf16 v[76:79], v[160:163], v[168:171], v[76:79]
	s_setprio 0
	s_setprio 1
	v_mfma_f32_16x16x32_bf16 v[120:123], v[132:135], v[188:191], v[120:123]
	v_mfma_f32_16x16x32_bf16 v[116:119], v[140:143], v[188:191], v[116:119]
	v_mfma_f32_16x16x32_bf16 v[104:107], v[132:135], v[180:183], v[104:107]
	v_mfma_f32_16x16x32_bf16 v[100:103], v[140:143], v[180:183], v[100:103]
	v_mfma_f32_16x16x32_bf16 v[88:91], v[132:135], v[172:175], v[88:91]
	v_mfma_f32_16x16x32_bf16 v[84:87], v[140:143], v[172:175], v[84:87]
	v_mfma_f32_16x16x32_bf16 v[72:75], v[132:135], v[164:167], v[72:75]
	v_mfma_f32_16x16x32_bf16 v[68:71], v[140:143], v[164:167], v[68:71]
	v_mfma_f32_16x16x32_bf16 v[120:123], v[136:139], v[192:195], v[120:123]
	v_mfma_f32_16x16x32_bf16 v[116:119], v[144:147], v[192:195], v[116:119]
	v_mfma_f32_16x16x32_bf16 v[104:107], v[136:139], v[184:187], v[104:107]
	v_mfma_f32_16x16x32_bf16 v[100:103], v[144:147], v[184:187], v[100:103]
	v_mfma_f32_16x16x32_bf16 v[88:91], v[136:139], v[176:179], v[88:91]
	v_mfma_f32_16x16x32_bf16 v[84:87], v[144:147], v[176:179], v[84:87]
	v_mfma_f32_16x16x32_bf16 v[72:75], v[136:139], v[168:171], v[72:75]
	v_mfma_f32_16x16x32_bf16 v[68:71], v[144:147], v[168:171], v[68:71]
	s_setprio 0
	s_barrier
	s_mov_b32 m0, s75
	v_lshl_add_u64 v[222:223], s[36:37], 0, v[198:199]
	s_add_u32 s10, s36, 0x40000
	ds_read_b128 v[188:191], v226 offset:16384
	ds_read_b128 v[192:195], v226 offset:17408
	ds_read_b128 v[180:183], v226 offset:18432
	ds_read_b128 v[184:187], v226 offset:19456
	ds_read_b128 v[172:175], v226 offset:20480
	ds_read_b128 v[176:179], v226 offset:21504
	ds_read_b128 v[164:167], v226 offset:22528
	ds_read_b128 v[168:171], v226 offset:23552
	global_load_lds_dwordx4 v[222:223], off
	v_lshl_add_u64 v[220:221], s[36:37], 0, v[202:203]
	s_mov_b32 m0, s84
	s_addc_u32 s11, s37, 0
	global_load_lds_dwordx4 v[220:221], off
	v_lshl_add_u64 v[216:217], s[10:11], 0, v[198:199]
	s_mov_b32 m0, s85
	v_lshl_add_u64 v[218:219], s[66:67], 0, v[200:201]
	global_load_lds_dwordx4 v[216:217], off
	v_lshl_add_u64 v[216:217], s[10:11], 0, v[202:203]
	s_mov_b32 m0, s86
	s_mov_b64 s[26:27], -1
	global_load_lds_dwordx4 v[216:217], off
	v_lshl_add_u64 v[216:217], s[66:67], 0, v[196:197]
	s_mov_b32 m0, s74
	s_and_b64 vcc, exec, s[68:69]
	global_load_lds_dwordx4 v[216:217], off
	s_mov_b32 m0, s87
	s_nop 0
	global_load_lds_dwordx4 v[218:219], off
	global_load_dword v227, v[230:231], off
	s_cbranch_vccz .LBB0_806
	s_waitcnt vmcnt(10)
	s_mov_b64 s[26:27], 0
